# v103 + P3 step: barrier moved before the PV MFMAs; 4 of the next tile's 8 K fragments read right after the barrier under the PV MFMAs, next step's QK chain starts with them
# baseline (speedup 1.0000x reference)
; #define LAS __attribute__((address_space(3)))
; __device__ __forceinline__ void attn_phase_mfma(Frame& F) {
;     ...
; #pragma unroll
;                 for (int r = 0; r < 16; ++r) s[r] = 0.f;
;                 bf16x8 kf[8];
; #pragma unroll
;                 for (int ks = 0; ks < 8; ++ks) kf[ks] = *(const LAS bf16x8*)(KB + c * AT_KPITCH + (16 * ks + 8 * hh) * 2);
;                 __builtin_amdgcn_sched_barrier(0);
; #pragma unroll
;                 for (int ks = 0; ks < 8; ++ks) s = __builtin_amdgcn_mfma_f32_32x32x16_bf16(kf[ks], qf[ks], s, 0, 0, 0);
;                 v4u vfr[4][2];
; #pragma unroll
;                 for (int db = 0; db < 4; ++db)
; #pragma unroll
;                     for (int s2 = 0; s2 < 2; ++s2) { const LAS unsigned char* vp = VB + (32 * db + c) * AT_VPITCH + (16 * s2 + 4 * hh) * 2;
;                         const v2u lo = *(const LAS v2u*)vp, hi = *(const LAS v2u*)(vp + 16); vfr[db][s2] = (v4u){lo.x, lo.y, hi.x, hi.y}; }
;                 __builtin_amdgcn_sched_barrier(0);
;     ...
;             if (kt + 2 <= qb) { AT_WRITE_TILE((st + 1) & 1); mw = mwn; }
;             if (kt + 4 <= qb) AT_LOAD_TILE(kt + 4);
.Lp3e_vrest:
	ds_read2_b64 v[152:155], v81 offset0:32 offset1:34
	ds_read2_b64 v[156:159], v81 offset0:36 offset1:38
	v_add_u32_e32 v81, 0x9800, v80
	v_add_u32_e32 v80, 0xa000, v80
	ds_read2_b64 v[164:167], v81 offset0:64 offset1:66
	ds_read2_b64 v[168:171], v81 offset0:68 offset1:70
	ds_read2_b64 v[172:175], v80 offset0:96 offset1:98
	ds_read2_b64 v[160:163], v80 offset0:100 offset1:102
	v_lshrrev_b32_e32 v233, v222, v229
	v_and_b32_e32 v199, 1, v233
	v_and_b32_e32 v198, 2, v233
	v_and_b32_e32 v242, 4, v233
	v_and_b32_e32 v250, 8, v233
	v_and_b32_e32 v249, 0x100, v233
	v_and_b32_e32 v248, 0x200, v233
	v_and_b32_e32 v244, 0x400, v233
	v_and_b32_e32 v243, 0x800, v233
	v_and_b32_e32 v241, 0x10000, v233
	v_and_b32_e32 v240, 0x20000, v233
	v_and_b32_e32 v239, 0x40000, v233
	v_and_b32_e32 v238, 0x80000, v233
	v_and_b32_e32 v237, 0x1000000, v233
	v_and_b32_e32 v236, 0x2000000, v233
	v_and_b32_e32 v235, 0x4000000, v233
	s_cmp_gt_i32 s15, s12
	s_cbranch_scc1 .Lp3e_nowrite
	s_xor_b32 s36, s18, 1
	s_mul_i32 s37, s36, 0x2200
	s_mulk_i32 s36, 0x2400
	v_add_u32_e32 v82, s37, v224
	s_waitcnt vmcnt(3)
	ds_write_b128 v82, v[96:99]
	s_waitcnt vmcnt(2)
	ds_write_b128 v82, v[100:103] offset:4352
	s_waitcnt vmcnt(1)
	v_and_b32_e32 v82, 0xffff, v104
	v_add_u32_e32 v83, s36, v225
	v_lshrrev_b32_e32 v84, 16, v104
	s_waitcnt vmcnt(0)
	v_lshl_or_b32 v82, v108, 16, v82
	v_and_or_b32 v84, v108, s92, v84
	v_add_u32_e32 v83, 0x8800, v83
	ds_write2_b32 v83, v82, v84 offset1:18
	v_and_b32_e32 v82, 0xffff, v105
	v_lshrrev_b32_e32 v84, 16, v105
	v_lshl_or_b32 v82, v109, 16, v82
	v_and_or_b32 v84, v109, s92, v84
	ds_write2_b32 v83, v82, v84 offset0:36 offset1:54
	v_and_b32_e32 v82, 0xffff, v106
	v_lshrrev_b32_e32 v84, 16, v106
	v_lshl_or_b32 v82, v110, 16, v82
	v_and_or_b32 v84, v110, s92, v84
	ds_write2_b32 v83, v82, v84 offset0:72 offset1:90
	v_and_b32_e32 v82, 0xffff, v107
	v_lshrrev_b32_e32 v84, 16, v107
	v_lshl_or_b32 v82, v111, 16, v82
	v_and_or_b32 v84, v111, s92, v84
	v_mov_b32_e32 v229, v230
	ds_write2_b32 v83, v82, v84 offset0:108 offset1:126

; __device__ __forceinline__ unsigned cvt_pk_bf16(float lo, float hi) { const f32x2 v = {lo, hi}; return __builtin_bit_cast(unsigned, __builtin_convertvector(v, bf16x2_t)); }
; #define LAS __attribute__((address_space(3)))
; __device__ __forceinline__ void attn_phase_mfma(Frame& F) {
;     ...
;         for (int st = 0; st < nsteps; ++st) {
;             const int kt = 2 * st + grp; const bool valid = kt <= qb;
;             LAS unsigned char* KB = KB0 + (st & 1) * (32 * AT_KPITCH); LAS unsigned char* VB = VB0 + (st & 1) * (128 * AT_VPITCH);
;             if (valid) {
;                 const int key0 = kt * 32;
;                 f32x16 s;
; #pragma unroll
;                 for (int r = 0; r < 16; ++r) s[r] = 0.f;
;                 bf16x8 kf[8];
; #pragma unroll
;                 for (int ks = 0; ks < 8; ++ks) kf[ks] = *(const LAS bf16x8*)(KB + c * AT_KPITCH + (16 * ks + 8 * hh) * 2);
;                 __builtin_amdgcn_sched_barrier(0);
; #pragma unroll
;                 for (int ks = 0; ks < 8; ++ks) s = __builtin_amdgcn_mfma_f32_32x32x16_bf16(kf[ks], qf[ks], s, 0, 0, 0);
;     ...
;                 bf16x8 pf[2];
; #pragma unroll
;                 for (int s2 = 0; s2 < 2; ++s2) { v4u w; w.x = pg8::cvt_pk_bf16(s[8 * s2 + 0], s[8 * s2 + 1]); w.y = pg8::cvt_pk_bf16(s[8 * s2 + 2], s[8 * s2 + 3]); w.z = pg8::cvt_pk_bf16(s[8 * s2 + 4], s[8 * s2 + 5]); w.w = pg8::cvt_pk_bf16(s[8 * s2 + 6], s[8 * s2 + 7]); pf[s2] = __builtin_bit_cast(bf16x8, w); }
; #pragma unroll
;                 for (int db = 0; db < 4; ++db)
; #pragma unroll
;                     for (int s2 = 0; s2 < 2; ++s2) o[db] = __builtin_amdgcn_mfma_f32_32x32x16_bf16(__builtin_bit_cast(bf16x8, vfr[db][s2]), pf[s2], o[db], 0, 0, 0);
;             }
;             if (kt + 2 <= qb) { AT_WRITE_TILE((st + 1) & 1); mw = mwn; }
;             if (kt + 4 <= qb) AT_LOAD_TILE(kt + 4);
;             asm volatile("s_waitcnt lgkmcnt(0)" ::: "memory"); __builtin_amdgcn_s_barrier(); asm volatile("" ::: "memory");
;         }
.LBB0_554:
	v_cvt_pk_bf16_f32 v64, v80, v81
	v_cvt_pk_bf16_f32 v65, v82, v83
	v_cvt_pk_bf16_f32 v66, v84, v85
	v_cvt_pk_bf16_f32 v67, v86, v87
	v_exp_f32_e32 v68, v95
	v_and_b32_e32 v69, 0x8000000, v233
	v_cmp_ne_u32_e32 vcc, 0, v69
	v_cvt_pk_bf16_f32 v69, v90, v91
	v_cvt_pk_bf16_f32 v70, v92, v93
	v_cndmask_b32_e32 v72, 0, v68, vcc
	v_cvt_pk_bf16_f32 v68, v88, v89
	v_cvt_pk_bf16_f32 v71, v94, v72
	v_add_f32_e32 v197, v247, v72
	v_add_f32_e32 v210, v197, v210
	s_waitcnt lgkmcnt(0)
	s_barrier
	s_add_i32 s36, s13, s14
	s_cmp_eq_u32 s36, 64
	s_cbranch_scc1 .Lp3e_pv_plain
	s_add_i32 s36, s15, 2
	s_cmp_gt_u32 s36, s10
	s_cbranch_scc1 .Lp3e_pv_plain
	s_xor_b32 s36, s18, 1
	s_mul_i32 s36, s36, 0x2200
	v_add_u32_e32 v196, s36, v221
	ds_read_b128 v[80:83], v196 offset:32
	ds_read_b128 v[84:87], v196 offset:64
	ds_read_b128 v[88:91], v196 offset:96
	ds_read_b128 v[92:95], v196 offset:128
	v_mfma_f32_32x32x16_bf16 v[48:63], v[148:151], v[64:67], v[48:63]
	v_mfma_f32_32x32x16_bf16 v[32:47], v[152:155], v[64:67], v[32:47]
	v_mfma_f32_32x32x16_bf16 v[16:31], v[164:167], v[64:67], v[16:31]
	v_mfma_f32_32x32x16_bf16 v[0:15], v[172:175], v[64:67], v[0:15]
	v_mfma_f32_32x32x16_bf16 v[48:63], v[144:147], v[68:71], v[48:63]
	v_mfma_f32_32x32x16_bf16 v[32:47], v[156:159], v[68:71], v[32:47]
	v_mfma_f32_32x32x16_bf16 v[16:31], v[168:171], v[68:71], v[16:31]
	v_mfma_f32_32x32x16_bf16 v[0:15], v[160:163], v[68:71], v[0:15]
	s_sub_i32 s14, s14, 64
	s_add_i32 s17, s17, 1
	s_add_i32 s16, s16, 64
	s_mov_b64 s[2:3], 0xd8000
	s_add_i32 s15, s15, 2
	v_lshl_add_u64 v[212:213], v[212:213], 0, 8
	v_lshl_add_u64 v[218:219], v[218:219], 0, s[2:3]
	v_lshl_add_u64 v[216:217], v[216:217], 0, s[2:3]
	v_lshl_add_u64 v[214:215], v[214:215], 0, s[2:3]
	v_mov_b32_e32 v234, v232
	s_and_b32 s18, s17, 1
	s_mul_i32 s0, s18, 0x2200
	v_add_u32_e32 v68, s0, v221
	ds_read_b128 v[156:159], v68
	ds_read_b128 v[144:147], v68 offset:160
	ds_read_b128 v[148:151], v68 offset:192
	ds_read_b128 v[152:155], v68 offset:224
	s_waitcnt lgkmcnt(7)
	v_mfma_f32_32x32x16_bf16 v[64:79], v[80:83], v[112:115], 0
	s_mul_i32 s0, s18, 0x2400
	s_waitcnt lgkmcnt(6)
	v_mfma_f32_32x32x16_bf16 v[64:79], v[84:87], v[116:119], v[64:79]
	v_add_u32_e32 v80, s0, v226
	v_add_u32_e32 v81, 0x8800, v80
	s_waitcnt lgkmcnt(5)
	v_mfma_f32_32x32x16_bf16 v[64:79], v[88:91], v[120:123], v[64:79]
	s_waitcnt lgkmcnt(4)
	v_mfma_f32_32x32x16_bf16 v[64:79], v[92:95], v[124:127], v[64:79]
	s_waitcnt lgkmcnt(3)
	v_mfma_f32_32x32x16_bf16 v[64:79], v[156:159], v[136:139], v[64:79]
	s_waitcnt lgkmcnt(2)
	v_mfma_f32_32x32x16_bf16 v[64:79], v[144:147], v[128:131], v[64:79]
	s_waitcnt lgkmcnt(1)
	v_mfma_f32_32x32x16_bf16 v[64:79], v[148:151], v[132:135], v[64:79]
	ds_read2_b64 v[148:151], v81 offset1:2
	ds_read2_b64 v[144:147], v81 offset0:4 offset1:6
	v_add_u32_e32 v81, 0x9000, v80
	s_waitcnt lgkmcnt(2)
	v_mfma_f32_32x32x16_bf16 v[64:79], v[152:155], v[140:143], v[64:79]
	s_branch .Lp3e_vrest
.Lp3e_pv_plain:
	v_mfma_f32_32x32x16_bf16 v[48:63], v[148:151], v[64:67], v[48:63]
	v_mfma_f32_32x32x16_bf16 v[32:47], v[152:155], v[64:67], v[32:47]
	v_mfma_f32_32x32x16_bf16 v[16:31], v[164:167], v[64:67], v[16:31]
	v_mfma_f32_32x32x16_bf16 v[0:15], v[172:175], v[64:67], v[0:15]
	v_mfma_f32_32x32x16_bf16 v[48:63], v[144:147], v[68:71], v[48:63]
	v_mfma_f32_32x32x16_bf16 v[32:47], v[156:159], v[68:71], v[32:47]
	v_mfma_f32_32x32x16_bf16 v[16:31], v[168:171], v[68:71], v[16:31]
	v_mfma_f32_32x32x16_bf16 v[0:15], v[160:163], v[68:71], v[0:15]
	s_nop 7
	s_nop 7
	s_nop 7
	s_branch .Lp3e_tail

; __device__ __forceinline__ void attn_phase_mfma(Frame& F) {
;     ...
;         for (int st = 0; st < nsteps; ++st) {
;             const int kt = 2 * st + grp; const bool valid = kt <= qb;
;             LAS unsigned char* KB = KB0 + (st & 1) * (32 * AT_KPITCH); LAS unsigned char* VB = VB0 + (st & 1) * (128 * AT_VPITCH);
;             if (valid) {
;                 const int key0 = kt * 32;
;                 f32x16 s;
; #pragma unroll
;                 for (int r = 0; r < 16; ++r) s[r] = 0.f;
;                 bf16x8 kf[8];
; #pragma unroll
;                 for (int ks = 0; ks < 8; ++ks) kf[ks] = *(const LAS bf16x8*)(KB + c * AT_KPITCH + (16 * ks + 8 * hh) * 2);
;                 __builtin_amdgcn_sched_barrier(0);
; #pragma unroll
;                 for (int ks = 0; ks < 8; ++ks) s = __builtin_amdgcn_mfma_f32_32x32x16_bf16(kf[ks], qf[ks], s, 0, 0, 0);
;                 v4u vfr[4][2];
; #pragma unroll
;                 for (int db = 0; db < 4; ++db)
; #pragma unroll
;                     for (int s2 = 0; s2 < 2; ++s2) { const LAS unsigned char* vp = VB + (32 * db + c) * AT_VPITCH + (16 * s2 + 4 * hh) * 2;
;                         const v2u lo = *(const LAS v2u*)vp, hi = *(const LAS v2u*)(vp + 16); vfr[db][s2] = (v4u){lo.x, lo.y, hi.x, hi.y}; }
;                 __builtin_amdgcn_sched_barrier(0);
;                 const bool far = (q0 - key0 - 31) >= 128;
;                 const unsigned mwh = mw >> (4 * hh);
;                 float mn, rs = 0.f;
;                 if (far) {
;                     float smax = fmaxf(fmaxf(s[0], s[1]), fmaxf(s[2], s[3]));
; #pragma unroll
;                     for (int r = 4; r < 16; r += 2) smax = fmaxf(smax, fmaxf(s[r], s[r + 1]));
;                     { float x0, x1; swap32(smax, x0, x1); smax = fmaxf(x0, x1); }
;                     mn = fmaxf(m, __builtin_fmaf(smax, C1, bfar));
;                     if (__all(mn - m <= AT_DEFER)) mn = m;
;                     const float bm = bfar - mn;
; #pragma unroll
;                     for (int r = 0; r < 16; ++r) { const float p = __builtin_amdgcn_exp2f(__builtin_fmaf(s[r], C1, bm));
;                         const float pmk = __builtin_bit_cast(float, __builtin_bit_cast(unsigned, p) & (unsigned)__builtin_amdgcn_sbfe((int)mwh, (r & 3) + 8 * (r >> 2), 1));
;                         s[r] = pmk; rs += pmk; }
;                 } else {
;                     float vmax = -INFINITY;
.Lp3e_tail:
	s_sub_i32 s14, s14, 64
	s_add_i32 s17, s17, 1
	s_add_i32 s0, s13, s14
	s_add_i32 s16, s16, 64
	s_mov_b64 s[2:3], 0xd8000
	s_add_i32 s15, s15, 2
	v_lshl_add_u64 v[212:213], v[212:213], 0, 8
	v_lshl_add_u64 v[218:219], v[218:219], 0, s[2:3]
	v_lshl_add_u64 v[216:217], v[216:217], 0, s[2:3]
	s_cmp_eq_u32 s0, 0
	v_lshl_add_u64 v[214:215], v[214:215], 0, s[2:3]
	s_cbranch_scc1 .LBB0_563
	v_mov_b32_e32 v234, v232
	s_and_b32 s18, s17, 1
	s_cmp_gt_u32 s15, s10
	s_cbranch_scc1 .LBB0_555
	s_branch .LBB0_550
